# grid barrier: waiters poll the top arrival counter (>= (gen+1)*nx) instead of the generation word
# baseline (speedup 1.0000x reference)
.LBB0_236:
	s_or_b64 exec, exec, s[8:9]
	v_cvt_f32_u32_e32 v5, v3
	s_waitcnt vmcnt(0)
	v_readfirstlane_b32 s2, v4
	v_sub_u32_e32 v4, 0, v3
	v_rcp_iflag_f32_e32 v5, v5
	v_add_u32_e32 v6, s2, v2
	v_mul_f32_e32 v5, 0x4f7ffffe, v5
	v_cvt_u32_f32_e32 v5, v5
	v_mul_lo_u32 v2, v4, v5
	v_mul_hi_u32 v2, v5, v2
	v_add_u32_e32 v2, v5, v2
	v_mul_hi_u32 v2, v6, v2
	v_mul_lo_u32 v4, v2, v3
	v_sub_u32_e32 v4, v6, v4
	v_add_u32_e32 v5, 1, v2
	v_cmp_ge_u32_e32 vcc, v4, v3
	s_nop 1
	v_cndmask_b32_e32 v2, v2, v5, vcc
	v_sub_u32_e32 v5, v4, v3
	v_cndmask_b32_e32 v4, v4, v5, vcc
	v_add_u32_e32 v5, 1, v2
	v_cmp_ge_u32_e32 vcc, v4, v3
	v_add_u32_e32 v4, 1, v6
	s_nop 0
	v_cndmask_b32_e32 v2, v2, v5, vcc
	v_mul_lo_u32 v5, v3, v2
	v_add_u32_e32 v3, v5, v3
	v_cmp_ne_u32_e32 vcc, v4, v3
	s_and_saveexec_b64 s[2:3], vcc
	s_xor_b64 s[6:7], exec, s[2:3]
	s_cbranch_execz .LBB0_252
	s_waitcnt lgkmcnt(0)
	v_add_u32_e32 v4, 1, v2
	v_mul_lo_u32 v4, v4, v1
	v_mov_b32_e32 v1, 0x7400
	global_load_dword v1, v1, s[84:85] sc1
	s_add_u32 s12, s84, 0x7400
	s_addc_u32 s13, s85, 0
	s_waitcnt vmcnt(0)
	v_cmp_gt_u32_e32 vcc, v4, v1
	s_and_saveexec_b64 s[8:9], vcc
	s_cbranch_execz .LBB0_251
	s_add_u32 s10, s84, 0x4200
	s_addc_u32 s11, s85, 0
	s_mov_b32 s2, 1
	s_mov_b64 s[14:15], 0
	v_mov_b32_e32 v1, 0
	s_branch .LBB0_240

.LBB0_242:
	global_load_dword v3, v1, s[12:13] sc1
	s_add_i32 s2, s2, 1
	s_mov_b64 s[20:21], -1
	s_waitcnt vmcnt(0)
	v_cmp_le_u32_e32 vcc, v4, v3
	s_orn2_b64 s[18:19], vcc, exec
	s_branch .LBB0_239

.LBB0_255:
	s_or_b64 exec, exec, s[8:9]
	v_cvt_f32_u32_e32 v4, v1
	s_waitcnt vmcnt(0)
	v_readfirstlane_b32 s2, v3
	s_add_u32 s8, s84, 0x7400
	s_addc_u32 s9, s85, 0
	s_add_u32 s100, s84, 0x7500
	s_addc_u32 s101, s85, 0
	v_rcp_iflag_f32_e32 v4, v4
	v_add_u32_e32 v2, s2, v2
	v_add_u32_e32 v5, 1, v2
	s_mov_b64 s[10:11], -1
	v_mul_f32_e32 v3, 0x4f7ffffe, v4
	v_cvt_u32_f32_e32 v3, v3
	v_sub_u32_e32 v4, 0, v1
	v_mul_lo_u32 v4, v4, v3
	v_mul_hi_u32 v4, v3, v4
	v_add_u32_e32 v3, v3, v4
	v_mul_hi_u32 v3, v2, v3
	v_mul_lo_u32 v4, v3, v1
	v_sub_u32_e32 v2, v2, v4
	v_add_u32_e32 v6, 1, v3
	v_cmp_ge_u32_e32 vcc, v2, v1
	v_sub_u32_e32 v4, v2, v1
	s_nop 0
	v_cndmask_b32_e32 v3, v3, v6, vcc
	v_cndmask_b32_e32 v2, v2, v4, vcc
	v_add_u32_e32 v4, 1, v3
	v_cmp_ge_u32_e32 vcc, v2, v1
	s_nop 1
	v_cndmask_b32_e32 v4, v3, v4, vcc
	v_mul_lo_u32 v2, v1, v4
	v_add_u32_e32 v1, v2, v1
	v_mov_b32_e32 v6, v1
	v_cmp_ne_u32_e32 vcc, v5, v1
	v_mov_b64_e32 v[2:3], s[100:101]
	s_and_saveexec_b64 s[6:7], vcc
	s_cbranch_execz .LBB0_267
	v_mov_b32_e32 v1, 0
	global_load_dword v2, v1, s[8:9] sc1
	s_mov_b64 s[14:15], 0
	s_waitcnt vmcnt(0)
	v_cmp_gt_u32_e32 vcc, v6, v2
	s_and_saveexec_b64 s[12:13], vcc
	s_cbranch_execz .LBB0_266
	s_add_u32 s10, s84, 0x4200
	s_addc_u32 s11, s85, 0
	s_mov_b32 s2, 1
	s_branch .LBB0_259

.LBB0_261:
	global_load_dword v2, v1, s[8:9] sc1
	s_add_i32 s2, s2, 1
	s_mov_b64 s[18:19], -1
	s_waitcnt vmcnt(0)
	v_cmp_le_u32_e32 vcc, v6, v2
	s_orn2_b64 s[22:23], vcc, exec
	s_branch .LBB0_258

.LBB0_784:
	s_or_b64 exec, exec, s[10:11]
	v_cvt_f32_u32_e32 v5, v3
	s_waitcnt vmcnt(0)
	v_readfirstlane_b32 s8, v4
	v_sub_u32_e32 v4, 0, v3
	v_rcp_iflag_f32_e32 v5, v5
	v_add_u32_e32 v6, s8, v2
	v_mul_f32_e32 v5, 0x4f7ffffe, v5
	v_cvt_u32_f32_e32 v5, v5
	v_mul_lo_u32 v2, v4, v5
	v_mul_hi_u32 v2, v5, v2
	v_add_u32_e32 v2, v5, v2
	v_mul_hi_u32 v2, v6, v2
	v_mul_lo_u32 v4, v2, v3
	v_sub_u32_e32 v4, v6, v4
	v_add_u32_e32 v5, 1, v2
	v_cmp_ge_u32_e32 vcc, v4, v3
	s_nop 1
	v_cndmask_b32_e32 v2, v2, v5, vcc
	v_sub_u32_e32 v5, v4, v3
	v_cndmask_b32_e32 v4, v4, v5, vcc
	v_add_u32_e32 v5, 1, v2
	v_cmp_ge_u32_e32 vcc, v4, v3
	v_add_u32_e32 v4, 1, v6
	s_nop 0
	v_cndmask_b32_e32 v2, v2, v5, vcc
	v_mul_lo_u32 v5, v3, v2
	v_add_u32_e32 v3, v5, v3
	v_cmp_ne_u32_e32 vcc, v4, v3
	s_and_saveexec_b64 s[8:9], vcc
	s_xor_b64 s[8:9], exec, s[8:9]
	s_cbranch_execz .LBB0_798
	s_waitcnt lgkmcnt(0)
	v_add_u32_e32 v4, 1, v2
	v_mul_lo_u32 v4, v4, v1
	v_mov_b32_e32 v1, 0x7400
	global_load_dword v1, v1, s[84:85] sc1
	s_add_u32 s14, s84, 0x7400
	s_addc_u32 s15, s85, 0
	s_waitcnt vmcnt(0)
	v_cmp_gt_u32_e32 vcc, v4, v1
	s_and_saveexec_b64 s[10:11], vcc
	s_cbranch_execz .LBB0_797
	s_add_u32 s12, s84, 0x4200
	s_addc_u32 s13, s85, 0
	s_mov_b32 s26, 1
	s_mov_b64 s[16:17], 0
	v_mov_b32_e32 v1, 0
	s_branch .LBB0_788

.LBB0_790:
	global_load_dword v3, v1, s[14:15] sc1
	s_add_i32 s26, s26, 1
	s_mov_b64 s[22:23], -1
	s_waitcnt vmcnt(0)
	v_cmp_le_u32_e32 vcc, v4, v3
	s_orn2_b64 s[20:21], vcc, exec
	s_branch .LBB0_787

.LBB0_801:
	s_or_b64 exec, exec, s[10:11]
	v_cvt_f32_u32_e32 v4, v1
	s_waitcnt vmcnt(0)
	v_readfirstlane_b32 s8, v3
	s_add_u32 s10, s84, 0x7400
	s_addc_u32 s11, s85, 0
	s_add_u32 s100, s84, 0x7500
	s_addc_u32 s101, s85, 0
	v_rcp_iflag_f32_e32 v4, v4
	v_add_u32_e32 v2, s8, v2
	v_add_u32_e32 v5, 1, v2
	s_mov_b64 s[12:13], -1
	v_mul_f32_e32 v3, 0x4f7ffffe, v4
	v_cvt_u32_f32_e32 v3, v3
	v_sub_u32_e32 v4, 0, v1
	v_mul_lo_u32 v4, v4, v3
	v_mul_hi_u32 v4, v3, v4
	v_add_u32_e32 v3, v3, v4
	v_mul_hi_u32 v3, v2, v3
	v_mul_lo_u32 v4, v3, v1
	v_sub_u32_e32 v2, v2, v4
	v_add_u32_e32 v6, 1, v3
	v_cmp_ge_u32_e32 vcc, v2, v1
	v_sub_u32_e32 v4, v2, v1
	s_nop 0
	v_cndmask_b32_e32 v3, v3, v6, vcc
	v_cndmask_b32_e32 v2, v2, v4, vcc
	v_add_u32_e32 v4, 1, v3
	v_cmp_ge_u32_e32 vcc, v2, v1
	s_nop 1
	v_cndmask_b32_e32 v4, v3, v4, vcc
	v_mul_lo_u32 v2, v1, v4
	v_add_u32_e32 v1, v2, v1
	v_mov_b32_e32 v6, v1
	v_cmp_ne_u32_e32 vcc, v5, v1
	v_mov_b64_e32 v[2:3], s[100:101]
	s_and_saveexec_b64 s[8:9], vcc
	s_cbranch_execz .LBB0_813
	v_mov_b32_e32 v1, 0
	global_load_dword v2, v1, s[10:11] sc1
	s_mov_b64 s[16:17], 0
	s_waitcnt vmcnt(0)
	v_cmp_gt_u32_e32 vcc, v6, v2
	s_and_saveexec_b64 s[14:15], vcc
	s_cbranch_execz .LBB0_812
	s_add_u32 s12, s84, 0x4200
	s_addc_u32 s13, s85, 0
	s_mov_b32 s26, 1
	s_branch .LBB0_805

.LBB0_807:
	global_load_dword v2, v1, s[10:11] sc1
	s_add_i32 s26, s26, 1
	s_mov_b64 s[20:21], -1
	s_waitcnt vmcnt(0)
	v_cmp_le_u32_e32 vcc, v6, v2
	s_orn2_b64 s[24:25], vcc, exec
	s_branch .LBB0_804

.LBB0_952:
	s_or_b64 exec, exec, s[8:9]
	v_cvt_f32_u32_e32 v5, v3
	s_waitcnt vmcnt(0)
	v_readfirstlane_b32 s6, v4
	v_sub_u32_e32 v4, 0, v3
	v_rcp_iflag_f32_e32 v5, v5
	v_add_u32_e32 v6, s6, v2
	v_mul_f32_e32 v5, 0x4f7ffffe, v5
	v_cvt_u32_f32_e32 v5, v5
	v_mul_lo_u32 v2, v4, v5
	v_mul_hi_u32 v2, v5, v2
	v_add_u32_e32 v2, v5, v2
	v_mul_hi_u32 v2, v6, v2
	v_mul_lo_u32 v4, v2, v3
	v_sub_u32_e32 v4, v6, v4
	v_add_u32_e32 v5, 1, v2
	v_cmp_ge_u32_e32 vcc, v4, v3
	s_nop 1
	v_cndmask_b32_e32 v2, v2, v5, vcc
	v_sub_u32_e32 v5, v4, v3
	v_cndmask_b32_e32 v4, v4, v5, vcc
	v_add_u32_e32 v5, 1, v2
	v_cmp_ge_u32_e32 vcc, v4, v3
	v_add_u32_e32 v4, 1, v6
	s_nop 0
	v_cndmask_b32_e32 v2, v2, v5, vcc
	v_mul_lo_u32 v5, v3, v2
	v_add_u32_e32 v3, v5, v3
	v_cmp_ne_u32_e32 vcc, v4, v3
	s_and_saveexec_b64 s[6:7], vcc
	s_xor_b64 s[6:7], exec, s[6:7]
	s_cbranch_execz .LBB0_966
	s_waitcnt lgkmcnt(0)
	v_add_u32_e32 v4, 1, v2
	v_mul_lo_u32 v4, v4, v1
	v_mov_b32_e32 v1, 0x7400
	global_load_dword v1, v1, s[84:85] sc1
	s_add_u32 s12, s84, 0x7400
	s_addc_u32 s13, s85, 0
	s_waitcnt vmcnt(0)
	v_cmp_gt_u32_e32 vcc, v4, v1
	s_and_saveexec_b64 s[8:9], vcc
	s_cbranch_execz .LBB0_965
	s_add_u32 s10, s84, 0x4200
	s_addc_u32 s11, s85, 0
	s_mov_b32 s24, 1
	s_mov_b64 s[14:15], 0
	v_mov_b32_e32 v1, 0
	s_branch .LBB0_956

.LBB0_958:
	global_load_dword v3, v1, s[12:13] sc1
	s_add_i32 s24, s24, 1
	s_mov_b64 s[20:21], -1
	s_waitcnt vmcnt(0)
	v_cmp_le_u32_e32 vcc, v4, v3
	s_orn2_b64 s[18:19], vcc, exec
	s_branch .LBB0_955

.LBB0_969:
	s_or_b64 exec, exec, s[8:9]
	v_cvt_f32_u32_e32 v4, v1
	s_waitcnt vmcnt(0)
	v_readfirstlane_b32 s6, v3
	s_add_u32 s8, s84, 0x7400
	s_addc_u32 s9, s85, 0
	s_add_u32 s100, s84, 0x7500
	s_addc_u32 s101, s85, 0
	v_rcp_iflag_f32_e32 v4, v4
	v_add_u32_e32 v2, s6, v2
	v_add_u32_e32 v5, 1, v2
	s_mov_b64 s[10:11], -1
	v_mul_f32_e32 v3, 0x4f7ffffe, v4
	v_cvt_u32_f32_e32 v3, v3
	v_sub_u32_e32 v4, 0, v1
	v_mul_lo_u32 v4, v4, v3
	v_mul_hi_u32 v4, v3, v4
	v_add_u32_e32 v3, v3, v4
	v_mul_hi_u32 v3, v2, v3
	v_mul_lo_u32 v4, v3, v1
	v_sub_u32_e32 v2, v2, v4
	v_add_u32_e32 v6, 1, v3
	v_cmp_ge_u32_e32 vcc, v2, v1
	v_sub_u32_e32 v4, v2, v1
	s_nop 0
	v_cndmask_b32_e32 v3, v3, v6, vcc
	v_cndmask_b32_e32 v2, v2, v4, vcc
	v_add_u32_e32 v4, 1, v3
	v_cmp_ge_u32_e32 vcc, v2, v1
	s_nop 1
	v_cndmask_b32_e32 v4, v3, v4, vcc
	v_mul_lo_u32 v2, v1, v4
	v_add_u32_e32 v1, v2, v1
	v_mov_b32_e32 v6, v1
	v_cmp_ne_u32_e32 vcc, v5, v1
	v_mov_b64_e32 v[2:3], s[100:101]
	s_and_saveexec_b64 s[6:7], vcc
	s_cbranch_execz .LBB0_981
	v_mov_b32_e32 v1, 0
	global_load_dword v2, v1, s[8:9] sc1
	s_mov_b64 s[14:15], 0
	s_waitcnt vmcnt(0)
	v_cmp_gt_u32_e32 vcc, v6, v2
	s_and_saveexec_b64 s[12:13], vcc
	s_cbranch_execz .LBB0_980
	s_add_u32 s10, s84, 0x4200
	s_addc_u32 s11, s85, 0
	s_mov_b32 s24, 1
	s_branch .LBB0_973

.LBB0_975:
	global_load_dword v2, v1, s[8:9] sc1
	s_add_i32 s24, s24, 1
	s_mov_b64 s[18:19], -1
	s_waitcnt vmcnt(0)
	v_cmp_le_u32_e32 vcc, v6, v2
	s_orn2_b64 s[22:23], vcc, exec
	s_branch .LBB0_972

.LBB0_1130:
	s_or_b64 exec, exec, s[12:13]
	v_cvt_f32_u32_e32 v5, v3
	s_waitcnt vmcnt(0)
	v_readfirstlane_b32 s10, v4
	v_sub_u32_e32 v4, 0, v3
	v_rcp_iflag_f32_e32 v5, v5
	v_add_u32_e32 v6, s10, v2
	v_mul_f32_e32 v5, 0x4f7ffffe, v5
	v_cvt_u32_f32_e32 v5, v5
	v_mul_lo_u32 v2, v4, v5
	v_mul_hi_u32 v2, v5, v2
	v_add_u32_e32 v2, v5, v2
	v_mul_hi_u32 v2, v6, v2
	v_mul_lo_u32 v4, v2, v3
	v_sub_u32_e32 v4, v6, v4
	v_add_u32_e32 v5, 1, v2
	v_cmp_ge_u32_e32 vcc, v4, v3
	s_nop 1
	v_cndmask_b32_e32 v2, v2, v5, vcc
	v_sub_u32_e32 v5, v4, v3
	v_cndmask_b32_e32 v4, v4, v5, vcc
	v_add_u32_e32 v5, 1, v2
	v_cmp_ge_u32_e32 vcc, v4, v3
	v_add_u32_e32 v4, 1, v6
	s_nop 0
	v_cndmask_b32_e32 v2, v2, v5, vcc
	v_mul_lo_u32 v5, v3, v2
	v_add_u32_e32 v3, v5, v3
	v_cmp_ne_u32_e32 vcc, v4, v3
	s_and_saveexec_b64 s[10:11], vcc
	s_xor_b64 s[10:11], exec, s[10:11]
	s_cbranch_execz .LBB0_1144
	s_waitcnt lgkmcnt(0)
	v_add_u32_e32 v4, 1, v2
	v_mul_lo_u32 v4, v4, v1
	v_mov_b32_e32 v1, 0x7400
	global_load_dword v1, v1, s[84:85] sc1
	s_add_u32 s16, s84, 0x7400
	s_addc_u32 s17, s85, 0
	s_waitcnt vmcnt(0)
	v_cmp_gt_u32_e32 vcc, v4, v1
	s_and_saveexec_b64 s[12:13], vcc
	s_cbranch_execz .LBB0_1143
	s_add_u32 s14, s84, 0x4200
	s_addc_u32 s15, s85, 0
	s_mov_b32 s28, 1
	s_mov_b64 s[18:19], 0
	v_mov_b32_e32 v1, 0
	s_branch .LBB0_1134

.LBB0_1136:
	global_load_dword v3, v1, s[16:17] sc1
	s_add_i32 s28, s28, 1
	s_mov_b64 s[24:25], -1
	s_waitcnt vmcnt(0)
	v_cmp_le_u32_e32 vcc, v4, v3
	s_orn2_b64 s[22:23], vcc, exec
	s_branch .LBB0_1133

.LBB0_1147:
	s_or_b64 exec, exec, s[12:13]
	v_cvt_f32_u32_e32 v4, v1
	s_waitcnt vmcnt(0)
	v_readfirstlane_b32 s10, v3
	s_add_u32 s12, s84, 0x7400
	s_addc_u32 s13, s85, 0
	s_add_u32 s100, s84, 0x7500
	s_addc_u32 s101, s85, 0
	v_rcp_iflag_f32_e32 v4, v4
	v_add_u32_e32 v2, s10, v2
	v_add_u32_e32 v5, 1, v2
	s_mov_b64 s[14:15], -1
	v_mul_f32_e32 v3, 0x4f7ffffe, v4
	v_cvt_u32_f32_e32 v3, v3
	v_sub_u32_e32 v4, 0, v1
	v_mul_lo_u32 v4, v4, v3
	v_mul_hi_u32 v4, v3, v4
	v_add_u32_e32 v3, v3, v4
	v_mul_hi_u32 v3, v2, v3
	v_mul_lo_u32 v4, v3, v1
	v_sub_u32_e32 v2, v2, v4
	v_add_u32_e32 v6, 1, v3
	v_cmp_ge_u32_e32 vcc, v2, v1
	v_sub_u32_e32 v4, v2, v1
	s_nop 0
	v_cndmask_b32_e32 v3, v3, v6, vcc
	v_cndmask_b32_e32 v2, v2, v4, vcc
	v_add_u32_e32 v4, 1, v3
	v_cmp_ge_u32_e32 vcc, v2, v1
	s_nop 1
	v_cndmask_b32_e32 v4, v3, v4, vcc
	v_mul_lo_u32 v2, v1, v4
	v_add_u32_e32 v1, v2, v1
	v_mov_b32_e32 v6, v1
	v_cmp_ne_u32_e32 vcc, v5, v1
	v_mov_b64_e32 v[2:3], s[100:101]
	s_and_saveexec_b64 s[10:11], vcc
	s_cbranch_execz .LBB0_1159
	v_mov_b32_e32 v1, 0
	global_load_dword v2, v1, s[12:13] sc1
	s_mov_b64 s[18:19], 0
	s_waitcnt vmcnt(0)
	v_cmp_gt_u32_e32 vcc, v6, v2
	s_and_saveexec_b64 s[16:17], vcc
	s_cbranch_execz .LBB0_1158
	s_add_u32 s14, s84, 0x4200
	s_addc_u32 s15, s85, 0
	s_mov_b32 s28, 1
	s_branch .LBB0_1151

.LBB0_1153:
	global_load_dword v2, v1, s[12:13] sc1
	s_add_i32 s28, s28, 1
	s_mov_b64 s[22:23], -1
	s_waitcnt vmcnt(0)
	v_cmp_le_u32_e32 vcc, v6, v2
	s_orn2_b64 s[26:27], vcc, exec
	s_branch .LBB0_1150

.LBB0_1284:
	s_or_b64 exec, exec, s[8:9]
	v_cvt_f32_u32_e32 v5, v3
	s_waitcnt vmcnt(0)
	v_readfirstlane_b32 s6, v4
	v_sub_u32_e32 v4, 0, v3
	v_rcp_iflag_f32_e32 v5, v5
	v_add_u32_e32 v6, s6, v2
	v_mul_f32_e32 v5, 0x4f7ffffe, v5
	v_cvt_u32_f32_e32 v5, v5
	v_mul_lo_u32 v2, v4, v5
	v_mul_hi_u32 v2, v5, v2
	v_add_u32_e32 v2, v5, v2
	v_mul_hi_u32 v2, v6, v2
	v_mul_lo_u32 v4, v2, v3
	v_sub_u32_e32 v4, v6, v4
	v_add_u32_e32 v5, 1, v2
	v_cmp_ge_u32_e32 vcc, v4, v3
	s_nop 1
	v_cndmask_b32_e32 v2, v2, v5, vcc
	v_sub_u32_e32 v5, v4, v3
	v_cndmask_b32_e32 v4, v4, v5, vcc
	v_add_u32_e32 v5, 1, v2
	v_cmp_ge_u32_e32 vcc, v4, v3
	v_add_u32_e32 v4, 1, v6
	s_nop 0
	v_cndmask_b32_e32 v2, v2, v5, vcc
	v_mul_lo_u32 v5, v3, v2
	v_add_u32_e32 v3, v5, v3
	v_cmp_ne_u32_e32 vcc, v4, v3
	s_and_saveexec_b64 s[6:7], vcc
	s_xor_b64 s[6:7], exec, s[6:7]
	s_cbranch_execz .LBB0_1298
	s_waitcnt lgkmcnt(0)
	v_add_u32_e32 v4, 1, v2
	v_mul_lo_u32 v4, v4, v1
	v_mov_b32_e32 v1, 0x7400
	global_load_dword v1, v1, s[84:85] sc1
	s_add_u32 s12, s84, 0x7400
	s_addc_u32 s13, s85, 0
	s_waitcnt vmcnt(0)
	v_cmp_gt_u32_e32 vcc, v4, v1
	s_and_saveexec_b64 s[8:9], vcc
	s_cbranch_execz .LBB0_1297
	s_add_u32 s10, s84, 0x4200
	s_addc_u32 s11, s85, 0
	s_mov_b32 s26, 1
	s_mov_b64 s[14:15], 0
	v_mov_b32_e32 v1, 0
	s_branch .LBB0_1288

.LBB0_1290:
	global_load_dword v3, v1, s[12:13] sc1
	s_add_i32 s26, s26, 1
	s_mov_b64 s[22:23], -1
	s_waitcnt vmcnt(0)
	v_cmp_le_u32_e32 vcc, v4, v3
	s_orn2_b64 s[20:21], vcc, exec
	s_branch .LBB0_1287

.LBB0_1301:
	s_or_b64 exec, exec, s[8:9]
	v_cvt_f32_u32_e32 v4, v1
	s_waitcnt vmcnt(0)
	v_readfirstlane_b32 s6, v3
	s_add_u32 s8, s84, 0x7400
	s_addc_u32 s9, s85, 0
	s_add_u32 s100, s84, 0x7500
	s_addc_u32 s101, s85, 0
	v_rcp_iflag_f32_e32 v4, v4
	v_add_u32_e32 v2, s6, v2
	v_add_u32_e32 v5, 1, v2
	s_mov_b64 s[10:11], -1
	v_mul_f32_e32 v3, 0x4f7ffffe, v4
	v_cvt_u32_f32_e32 v3, v3
	v_sub_u32_e32 v4, 0, v1
	v_mul_lo_u32 v4, v4, v3
	v_mul_hi_u32 v4, v3, v4
	v_add_u32_e32 v3, v3, v4
	v_mul_hi_u32 v3, v2, v3
	v_mul_lo_u32 v4, v3, v1
	v_sub_u32_e32 v2, v2, v4
	v_add_u32_e32 v6, 1, v3
	v_cmp_ge_u32_e32 vcc, v2, v1
	v_sub_u32_e32 v4, v2, v1
	s_nop 0
	v_cndmask_b32_e32 v3, v3, v6, vcc
	v_cndmask_b32_e32 v2, v2, v4, vcc
	v_add_u32_e32 v4, 1, v3
	v_cmp_ge_u32_e32 vcc, v2, v1
	s_nop 1
	v_cndmask_b32_e32 v4, v3, v4, vcc
	v_mul_lo_u32 v2, v1, v4
	v_add_u32_e32 v1, v2, v1
	v_mov_b32_e32 v6, v1
	v_cmp_ne_u32_e32 vcc, v5, v1
	v_mov_b64_e32 v[2:3], s[100:101]
	s_and_saveexec_b64 s[6:7], vcc
	s_cbranch_execz .LBB0_1313
	v_mov_b32_e32 v1, 0
	global_load_dword v2, v1, s[8:9] sc1
	s_mov_b64 s[14:15], 0
	s_waitcnt vmcnt(0)
	v_cmp_gt_u32_e32 vcc, v6, v2
	s_and_saveexec_b64 s[12:13], vcc
	s_cbranch_execz .LBB0_1312
	s_add_u32 s10, s84, 0x4200
	s_addc_u32 s11, s85, 0
	s_mov_b32 s26, 1
	s_branch .LBB0_1305

.LBB0_1307:
	global_load_dword v2, v1, s[8:9] sc1
	s_add_i32 s26, s26, 1
	s_mov_b64 s[20:21], -1
	s_waitcnt vmcnt(0)
	v_cmp_le_u32_e32 vcc, v6, v2
	s_orn2_b64 s[24:25], vcc, exec
	s_branch .LBB0_1304
